# speedup vs baseline: 1.0852x; 1.0082x over previous
.LBB1_13:
	v_add_u32_e32 v147, v149, v148
	ds_read_b128 v[180:183], v147
	ds_read_b128 v[184:187], v147 offset:1024
	ds_read_b128 v[188:191], v147 offset:256
	ds_read_b128 v[192:195], v147 offset:1280
	s_add_i32 s26, s22, s21
	v_add_u32_e32 v147, v162, v158
	v_add_u32_e32 v248, v162, v159
	v_add_u32_e32 v249, v162, v160
	v_add_u32_e32 v250, v162, v161
	ds_read_b128 v[196:199], v147
	ds_read_b128 v[200:203], v147 offset:1024
	ds_read_b128 v[204:207], v248
	ds_read_b128 v[208:211], v248 offset:1024
	ds_read_b128 v[212:215], v249
	ds_read_b128 v[216:219], v249 offset:1024
	ds_read_b128 v[220:223], v250
	ds_read_b128 v[224:227], v250 offset:1024
	s_waitcnt lgkmcnt(8)
	s_barrier
	s_waitcnt lgkmcnt(0)
	s_setprio 1
	s_waitcnt lgkmcnt(0)
	v_mfma_f32_16x16x32_f16 v[124:127], v[180:183], v[196:199], v[124:127]
	v_mfma_f32_16x16x32_f16 v[120:123], v[188:191], v[196:199], v[120:123]
	s_add_i32 s24, s26, 1
	s_ashr_i32 s25, s24, 31
	v_mfma_f32_16x16x32_f16 v[116:119], v[180:183], v[204:207], v[116:119]
	s_lshl_b64 s[24:25], s[24:25], 7
	v_add_u32_e32 v232, 0xc000, v163
	v_mfma_f32_16x16x32_f16 v[112:115], v[188:191], v[204:207], v[112:115]
	v_lshl_add_u64 v[228:229], v[138:139], 0, s[24:25]
	v_readfirstlane_b32 s24, v232
	v_mfma_f32_16x16x32_f16 v[108:111], v[180:183], v[212:215], v[108:111]
	v_add_u32_e32 v232, 0xe000, v163
	v_lshl_add_u64 v[230:231], v[228:229], 0, v[134:135]
	v_mfma_f32_16x16x32_f16 v[104:107], v[188:191], v[212:215], v[104:107]
	s_mov_b32 m0, s24
	v_readfirstlane_b32 s24, v232
	v_mfma_f32_16x16x32_f16 v[100:103], v[180:183], v[220:223], v[100:103]
	global_load_lds_dwordx4 v[230:231], off
	v_mfma_f32_16x16x32_f16 v[96:99], v[188:191], v[220:223], v[96:99]
	v_lshl_add_u64 v[228:229], v[228:229], 0, v[136:137]
	s_mov_b32 m0, s24
	v_mfma_f32_16x16x32_f16 v[124:127], v[184:187], v[200:203], v[124:127]
	global_load_lds_dwordx4 v[228:229], off
	v_mfma_f32_16x16x32_f16 v[120:123], v[192:195], v[200:203], v[120:123]
	v_mfma_f32_16x16x32_f16 v[116:119], v[184:187], v[208:211], v[116:119]
	v_mfma_f32_16x16x32_f16 v[112:115], v[192:195], v[208:211], v[112:115]
	v_mfma_f32_16x16x32_f16 v[108:111], v[184:187], v[216:219], v[108:111]
	v_mfma_f32_16x16x32_f16 v[104:107], v[192:195], v[216:219], v[104:107]
	v_mfma_f32_16x16x32_f16 v[100:103], v[184:187], v[224:227], v[100:103]
	v_mfma_f32_16x16x32_f16 v[96:99], v[192:195], v[224:227], v[96:99]
	s_setprio 0
	s_barrier
	s_add_i32 s24, s26, 2
	s_ashr_i32 s25, s24, 31
	s_lshl_b64 s[24:25], s[24:25], 7
	v_lshl_add_u64 v[244:245], v[140:141], 0, s[24:25]
	v_readfirstlane_b32 s27, v173
	v_add_u32_e32 v240, v150, v148
	v_lshl_add_u64 v[246:247], v[244:245], 0, v[134:135]
	s_mov_b32 m0, s27
	v_readfirstlane_b32 s27, v174
	ds_read_b128 v[228:231], v240
	ds_read_b128 v[232:235], v240 offset:1024
	ds_read_b128 v[236:239], v240 offset:256
	ds_read_b128 v[240:243], v240 offset:1280
	s_add_i32 s21, s21, 2
	s_barrier
	s_waitcnt lgkmcnt(0)
	s_setprio 1
	s_waitcnt lgkmcnt(0)
	v_mfma_f32_16x16x32_f16 v[92:95], v[228:231], v[196:199], v[92:95]
	v_mfma_f32_16x16x32_f16 v[88:91], v[236:239], v[196:199], v[88:91]
	global_load_lds_dwordx4 v[246:247], off
	v_mfma_f32_16x16x32_f16 v[84:87], v[228:231], v[204:207], v[84:87]
	v_lshl_add_u64 v[244:245], v[244:245], 0, v[136:137]
	s_mov_b32 m0, s27
	v_mfma_f32_16x16x32_f16 v[80:83], v[236:239], v[204:207], v[80:83]
	global_load_lds_dwordx4 v[244:245], off
	v_mfma_f32_16x16x32_f16 v[76:79], v[228:231], v[212:215], v[76:79]
	v_mfma_f32_16x16x32_f16 v[72:75], v[236:239], v[212:215], v[72:75]
	v_mfma_f32_16x16x32_f16 v[68:71], v[228:231], v[220:223], v[68:71]
	v_mfma_f32_16x16x32_f16 v[64:67], v[236:239], v[220:223], v[64:67]
	v_mfma_f32_16x16x32_f16 v[92:95], v[232:235], v[200:203], v[92:95]
	v_mfma_f32_16x16x32_f16 v[88:91], v[240:243], v[200:203], v[88:91]
	v_mfma_f32_16x16x32_f16 v[84:87], v[232:235], v[208:211], v[84:87]
	v_mfma_f32_16x16x32_f16 v[80:83], v[240:243], v[208:211], v[80:83]
	v_mfma_f32_16x16x32_f16 v[76:79], v[232:235], v[216:219], v[76:79]
	v_mfma_f32_16x16x32_f16 v[72:75], v[240:243], v[216:219], v[72:75]
	v_mfma_f32_16x16x32_f16 v[68:71], v[232:235], v[224:227], v[68:71]
	v_mfma_f32_16x16x32_f16 v[64:67], v[240:243], v[224:227], v[64:67]
	s_setprio 0
	v_lshl_add_u64 v[244:245], v[142:143], 0, s[24:25]
	v_readfirstlane_b32 s27, v163
	v_lshl_add_u64 v[246:247], v[244:245], 0, v[134:135]
	s_mov_b32 m0, s27
	v_readfirstlane_b32 s27, v164
	s_barrier
	ds_read_b128 v[196:199], v147 offset:16384
	ds_read_b128 v[200:203], v147 offset:17408
	ds_read_b128 v[204:207], v248 offset:16384
	ds_read_b128 v[208:211], v248 offset:17408
	ds_read_b128 v[212:215], v249 offset:16384
	ds_read_b128 v[216:219], v249 offset:17408
	ds_read_b128 v[220:223], v250 offset:16384
	ds_read_b128 v[224:227], v250 offset:17408
	s_barrier
	s_waitcnt lgkmcnt(0)
	s_setprio 1
	s_waitcnt lgkmcnt(0)
	v_mfma_f32_16x16x32_f16 v[60:63], v[180:183], v[196:199], v[60:63]
	v_mfma_f32_16x16x32_f16 v[56:59], v[188:191], v[196:199], v[56:59]
	v_mfma_f32_16x16x32_f16 v[52:55], v[180:183], v[204:207], v[52:55]
	v_mfma_f32_16x16x32_f16 v[48:51], v[188:191], v[204:207], v[48:51]
	v_mfma_f32_16x16x32_f16 v[44:47], v[180:183], v[212:215], v[44:47]
	v_mfma_f32_16x16x32_f16 v[40:43], v[188:191], v[212:215], v[40:43]
	v_mfma_f32_16x16x32_f16 v[36:39], v[180:183], v[220:223], v[36:39]
	v_mfma_f32_16x16x32_f16 v[32:35], v[188:191], v[220:223], v[32:35]
	v_mfma_f32_16x16x32_f16 v[60:63], v[184:187], v[200:203], v[60:63]
	v_mfma_f32_16x16x32_f16 v[56:59], v[192:195], v[200:203], v[56:59]
	v_mfma_f32_16x16x32_f16 v[52:55], v[184:187], v[208:211], v[52:55]
	v_mfma_f32_16x16x32_f16 v[48:51], v[192:195], v[208:211], v[48:51]
	v_mfma_f32_16x16x32_f16 v[44:47], v[184:187], v[216:219], v[44:47]
	v_mfma_f32_16x16x32_f16 v[40:43], v[192:195], v[216:219], v[40:43]
	v_mfma_f32_16x16x32_f16 v[36:39], v[184:187], v[224:227], v[36:39]
	v_mfma_f32_16x16x32_f16 v[32:35], v[192:195], v[224:227], v[32:35]
	s_setprio 0
	s_barrier
	global_load_lds_dwordx4 v[246:247], off
	v_lshl_add_u64 v[244:245], v[244:245], 0, v[136:137]
	s_mov_b32 m0, s27
	s_nop 0
	global_load_lds_dwordx4 v[244:245], off
	v_lshl_add_u64 v[180:181], v[144:145], 0, s[24:25]
	v_readfirstlane_b32 s27, v175
	v_lshl_add_u64 v[182:183], v[180:181], 0, v[134:135]
	s_mov_b32 m0, s27
	v_readfirstlane_b32 s27, v176
	global_load_lds_dwordx4 v[182:183], off
	v_lshl_add_u64 v[180:181], v[180:181], 0, v[136:137]
	s_mov_b32 m0, s27
	s_nop 0
	global_load_lds_dwordx4 v[180:181], off
	s_waitcnt vmcnt(6)
	s_barrier
	s_setprio 1
	v_mfma_f32_16x16x32_f16 v[28:31], v[228:231], v[196:199], v[28:31]
	v_mfma_f32_16x16x32_f16 v[24:27], v[236:239], v[196:199], v[24:27]
	v_mfma_f32_16x16x32_f16 v[20:23], v[228:231], v[204:207], v[20:23]
	v_mfma_f32_16x16x32_f16 v[16:19], v[236:239], v[204:207], v[16:19]
	v_mfma_f32_16x16x32_f16 v[12:15], v[228:231], v[212:215], v[12:15]
	v_mfma_f32_16x16x32_f16 v[8:11], v[236:239], v[212:215], v[8:11]
	v_mfma_f32_16x16x32_f16 v[4:7], v[228:231], v[220:223], v[4:7]
	v_mfma_f32_16x16x32_f16 v[0:3], v[236:239], v[220:223], v[0:3]
	v_mfma_f32_16x16x32_f16 v[28:31], v[232:235], v[200:203], v[28:31]
	v_mfma_f32_16x16x32_f16 v[24:27], v[240:243], v[200:203], v[24:27]
	v_mfma_f32_16x16x32_f16 v[20:23], v[232:235], v[208:211], v[20:23]
	v_mfma_f32_16x16x32_f16 v[16:19], v[240:243], v[208:211], v[16:19]
	v_mfma_f32_16x16x32_f16 v[12:15], v[232:235], v[216:219], v[12:15]
	v_mfma_f32_16x16x32_f16 v[8:11], v[240:243], v[216:219], v[8:11]
	v_mfma_f32_16x16x32_f16 v[4:7], v[232:235], v[224:227], v[4:7]
	v_mfma_f32_16x16x32_f16 v[0:3], v[240:243], v[224:227], v[0:3]
	s_setprio 0
	v_add_u32_e32 v192, v151, v148
	s_barrier
	ds_read_b128 v[180:183], v192
	ds_read_b128 v[184:187], v192 offset:1024
	ds_read_b128 v[188:191], v192 offset:256
	ds_read_b128 v[192:195], v192 offset:1280
	ds_read_b128 v[196:199], v147 offset:32768
	ds_read_b128 v[200:203], v147 offset:33792
	ds_read_b128 v[204:207], v248 offset:32768
	ds_read_b128 v[208:211], v248 offset:33792
	ds_read_b128 v[212:215], v249 offset:32768
	ds_read_b128 v[216:219], v249 offset:33792
	ds_read_b128 v[220:223], v250 offset:32768
	ds_read_b128 v[224:227], v250 offset:33792
	s_waitcnt lgkmcnt(8)
	s_barrier
	s_waitcnt lgkmcnt(0)
	s_setprio 1
	s_waitcnt lgkmcnt(0)
	v_mfma_f32_16x16x32_f16 v[124:127], v[180:183], v[196:199], v[124:127]
	v_mfma_f32_16x16x32_f16 v[120:123], v[188:191], v[196:199], v[120:123]
	v_mfma_f32_16x16x32_f16 v[116:119], v[180:183], v[204:207], v[116:119]
	v_lshl_add_u64 v[228:229], v[138:139], 0, s[24:25]
	v_readfirstlane_b32 s24, v165
	v_mfma_f32_16x16x32_f16 v[112:115], v[188:191], v[204:207], v[112:115]
	v_lshl_add_u64 v[230:231], v[228:229], 0, v[134:135]
	s_mov_b32 m0, s24
	v_mfma_f32_16x16x32_f16 v[108:111], v[180:183], v[212:215], v[108:111]
	v_readfirstlane_b32 s24, v166
	v_mfma_f32_16x16x32_f16 v[104:107], v[188:191], v[212:215], v[104:107]
	global_load_lds_dwordx4 v[230:231], off
	v_mfma_f32_16x16x32_f16 v[100:103], v[180:183], v[220:223], v[100:103]
	v_lshl_add_u64 v[228:229], v[228:229], 0, v[136:137]
	s_mov_b32 m0, s24
	v_mfma_f32_16x16x32_f16 v[96:99], v[188:191], v[220:223], v[96:99]
	global_load_lds_dwordx4 v[228:229], off
	v_mfma_f32_16x16x32_f16 v[124:127], v[184:187], v[200:203], v[124:127]
	v_mfma_f32_16x16x32_f16 v[120:123], v[192:195], v[200:203], v[120:123]
	v_mfma_f32_16x16x32_f16 v[116:119], v[184:187], v[208:211], v[116:119]
	v_mfma_f32_16x16x32_f16 v[112:115], v[192:195], v[208:211], v[112:115]
	v_mfma_f32_16x16x32_f16 v[108:111], v[184:187], v[216:219], v[108:111]
	v_mfma_f32_16x16x32_f16 v[104:107], v[192:195], v[216:219], v[104:107]
	v_mfma_f32_16x16x32_f16 v[100:103], v[184:187], v[224:227], v[100:103]
	v_mfma_f32_16x16x32_f16 v[96:99], v[192:195], v[224:227], v[96:99]
	s_setprio 0
	s_barrier
	s_add_i32 s24, s26, 3
	s_ashr_i32 s25, s24, 31
	s_lshl_b64 s[24:25], s[24:25], 7
	v_lshl_add_u64 v[244:245], v[140:141], 0, s[24:25]
	v_readfirstlane_b32 s26, v177
	v_add_u32_e32 v240, v152, v148
	v_lshl_add_u64 v[246:247], v[244:245], 0, v[134:135]
	s_mov_b32 m0, s26
	v_readfirstlane_b32 s26, v178
	ds_read_b128 v[228:231], v240
	ds_read_b128 v[232:235], v240 offset:1024
	ds_read_b128 v[236:239], v240 offset:256
	ds_read_b128 v[240:243], v240 offset:1280
	s_barrier
	s_waitcnt lgkmcnt(0)
	s_setprio 1
	s_waitcnt lgkmcnt(0)
	v_mfma_f32_16x16x32_f16 v[92:95], v[228:231], v[196:199], v[92:95]
	v_mfma_f32_16x16x32_f16 v[88:91], v[236:239], v[196:199], v[88:91]
	global_load_lds_dwordx4 v[246:247], off
	v_mfma_f32_16x16x32_f16 v[84:87], v[228:231], v[204:207], v[84:87]
	v_lshl_add_u64 v[244:245], v[244:245], 0, v[136:137]
	s_mov_b32 m0, s26
	v_mfma_f32_16x16x32_f16 v[80:83], v[236:239], v[204:207], v[80:83]
	global_load_lds_dwordx4 v[244:245], off
	v_mfma_f32_16x16x32_f16 v[76:79], v[228:231], v[212:215], v[76:79]
	v_mfma_f32_16x16x32_f16 v[72:75], v[236:239], v[212:215], v[72:75]
	v_mfma_f32_16x16x32_f16 v[68:71], v[228:231], v[220:223], v[68:71]
	v_mfma_f32_16x16x32_f16 v[64:67], v[236:239], v[220:223], v[64:67]
	v_mfma_f32_16x16x32_f16 v[92:95], v[232:235], v[200:203], v[92:95]
	v_mfma_f32_16x16x32_f16 v[88:91], v[240:243], v[200:203], v[88:91]
	v_mfma_f32_16x16x32_f16 v[84:87], v[232:235], v[208:211], v[84:87]
	v_mfma_f32_16x16x32_f16 v[80:83], v[240:243], v[208:211], v[80:83]
	v_mfma_f32_16x16x32_f16 v[76:79], v[232:235], v[216:219], v[76:79]
	v_mfma_f32_16x16x32_f16 v[72:75], v[240:243], v[216:219], v[72:75]
	v_mfma_f32_16x16x32_f16 v[68:71], v[232:235], v[224:227], v[68:71]
	v_mfma_f32_16x16x32_f16 v[64:67], v[240:243], v[224:227], v[64:67]
	s_setprio 0
	v_lshl_add_u64 v[244:245], v[142:143], 0, s[24:25]
	v_readfirstlane_b32 s26, v167
	v_lshl_add_u64 v[246:247], v[244:245], 0, v[134:135]
	s_mov_b32 m0, s26
	v_readfirstlane_b32 s26, v168
	s_barrier
	ds_read_b128 v[196:199], v147 offset:49152
	ds_read_b128 v[200:203], v147 offset:50176
	ds_read_b128 v[204:207], v248 offset:49152
	ds_read_b128 v[208:211], v248 offset:50176
	ds_read_b128 v[212:215], v249 offset:49152
	ds_read_b128 v[216:219], v249 offset:50176
	ds_read_b128 v[220:223], v250 offset:49152
	ds_read_b128 v[224:227], v250 offset:50176
	s_barrier
	s_waitcnt lgkmcnt(0)
	s_setprio 1
	s_waitcnt lgkmcnt(0)
	v_mfma_f32_16x16x32_f16 v[60:63], v[180:183], v[196:199], v[60:63]
	v_mfma_f32_16x16x32_f16 v[56:59], v[188:191], v[196:199], v[56:59]
	v_mfma_f32_16x16x32_f16 v[52:55], v[180:183], v[204:207], v[52:55]
	v_mfma_f32_16x16x32_f16 v[48:51], v[188:191], v[204:207], v[48:51]
	v_mfma_f32_16x16x32_f16 v[44:47], v[180:183], v[212:215], v[44:47]
	v_mfma_f32_16x16x32_f16 v[40:43], v[188:191], v[212:215], v[40:43]
	v_mfma_f32_16x16x32_f16 v[36:39], v[180:183], v[220:223], v[36:39]
	v_mfma_f32_16x16x32_f16 v[32:35], v[188:191], v[220:223], v[32:35]
	v_mfma_f32_16x16x32_f16 v[60:63], v[184:187], v[200:203], v[60:63]
	v_mfma_f32_16x16x32_f16 v[56:59], v[192:195], v[200:203], v[56:59]
	v_mfma_f32_16x16x32_f16 v[52:55], v[184:187], v[208:211], v[52:55]
	v_mfma_f32_16x16x32_f16 v[48:51], v[192:195], v[208:211], v[48:51]
	v_mfma_f32_16x16x32_f16 v[44:47], v[184:187], v[216:219], v[44:47]
	v_mfma_f32_16x16x32_f16 v[40:43], v[192:195], v[216:219], v[40:43]
	v_mfma_f32_16x16x32_f16 v[36:39], v[184:187], v[224:227], v[36:39]
	v_mfma_f32_16x16x32_f16 v[32:35], v[192:195], v[224:227], v[32:35]
	s_setprio 0
	s_barrier
	global_load_lds_dwordx4 v[246:247], off
	v_lshl_add_u64 v[244:245], v[244:245], 0, v[136:137]
	s_mov_b32 m0, s26
	s_nop 0
	global_load_lds_dwordx4 v[244:245], off
	v_lshl_add_u64 v[180:181], v[144:145], 0, s[24:25]
	v_readfirstlane_b32 s24, v179
	v_lshl_add_u64 v[182:183], v[180:181], 0, v[134:135]
	s_mov_b32 m0, s24
	v_readfirstlane_b32 s24, v146
	global_load_lds_dwordx4 v[182:183], off
	v_lshl_add_u64 v[180:181], v[180:181], 0, v[136:137]
	s_mov_b32 m0, s24
	s_nop 0
	global_load_lds_dwordx4 v[180:181], off
	s_waitcnt vmcnt(6)
	s_barrier
	s_setprio 1
	v_mfma_f32_16x16x32_f16 v[28:31], v[228:231], v[196:199], v[28:31]
	v_mfma_f32_16x16x32_f16 v[24:27], v[236:239], v[196:199], v[24:27]
	v_mfma_f32_16x16x32_f16 v[20:23], v[228:231], v[204:207], v[20:23]
	v_mfma_f32_16x16x32_f16 v[16:19], v[236:239], v[204:207], v[16:19]
	v_mfma_f32_16x16x32_f16 v[12:15], v[228:231], v[212:215], v[12:15]
	v_mfma_f32_16x16x32_f16 v[8:11], v[236:239], v[212:215], v[8:11]
	v_mfma_f32_16x16x32_f16 v[4:7], v[228:231], v[220:223], v[4:7]
	v_mfma_f32_16x16x32_f16 v[0:3], v[236:239], v[220:223], v[0:3]
	v_mfma_f32_16x16x32_f16 v[28:31], v[232:235], v[200:203], v[28:31]
	v_mfma_f32_16x16x32_f16 v[24:27], v[240:243], v[200:203], v[24:27]
	v_mfma_f32_16x16x32_f16 v[20:23], v[232:235], v[208:211], v[20:23]
	v_mfma_f32_16x16x32_f16 v[16:19], v[240:243], v[208:211], v[16:19]
	v_mfma_f32_16x16x32_f16 v[12:15], v[232:235], v[216:219], v[12:15]
	v_mfma_f32_16x16x32_f16 v[8:11], v[240:243], v[216:219], v[8:11]
	v_mfma_f32_16x16x32_f16 v[4:7], v[232:235], v[224:227], v[4:7]
	v_mfma_f32_16x16x32_f16 v[0:3], v[240:243], v[224:227], v[0:3]
	s_setprio 0
	s_cmp_ge_i32 s21, s5
	s_barrier
	s_cbranch_scc0 .LBB1_13
